# union 4: expert GEMM1 epilogue with the power-of-two descales folded into constants (2 multiplies and a copy fewer per element, no packed multiply)
# speedup vs baseline: 1.0040x; 1.0040x over previous
.LBB0_1044:
	s_lshl_b32 s4, s10, 2
	s_add_i32 s4, s4, 0
	s_add_i32 s4, s4, 0x20180
	v_mov_b32_e32 v2, v177
	v_mov_b32_e32 v4, v192
	v_mov_b32_e32 v3, s4
	s_nop 15
	s_nop 15
	ds_read_b32 v10, v3
	s_cmp_lt_i32 s10, 64
	v_add_u32_e32 v11, s53, v2
	v_mov_b32_e32 v9, 0x3b800000
	s_cselect_b64 s[38:39], -1, 0
	s_cmp_gt_i32 s10, 63
	v_mov_b32_e32 v5, 0x3b800000
	s_cbranch_scc1 .LBB0_1048
	v_add_u32_e32 v2, s14, v11
	s_waitcnt lgkmcnt(0)
	v_cmp_lt_i32_e32 vcc, v2, v10
	v_mov_b32_e32 v5, 0
	s_and_saveexec_b64 s[4:5], vcc
	s_cbranch_execz .LBB0_1047
	s_ashr_i32 s11, s10, 31
	s_lshl_b64 s[40:41], s[10:11], 15
	s_add_u32 s40, s51, s40
	s_addc_u32 s41, s52, s41
	v_ashrrev_i32_e32 v3, 31, v2
	v_lshl_add_u64 v[2:3], v[2:3], 2, s[40:41]
	global_load_dword v2, v[2:3], off
	s_waitcnt vmcnt(0)
	v_mul_f32_e32 v5, 0x3b800000, v2

.LBB0_1048:
	v_mul_f32_e32 v3, 0xbcb8aa3b, v158
	v_exp_f32_e32 v7, v3
	v_mul_f32_e32 v173, v158, v5
	v_mul_f32_e32 v12, 0xbcb8aa3b, v154
	v_add_f32_e32 v6, 1.0, v7
	v_rcp_f32_e32 v7, v6
	v_exp_f32_e32 v12, v12
	v_mul_f32_e32 v7, v7, v173
	v_mul_f32_e32 v173, v154, v5
	v_mul_f32_e32 v14, v150, v7
	v_add_f32_e32 v6, 1.0, v12
	v_rcp_f32_e32 v7, v6
	v_mul_f32_e32 v12, 0xbcb8aa3b, v159
	v_exp_f32_e32 v12, v12
	v_mul_f32_e32 v7, v7, v173
	v_mul_f32_e32 v173, v159, v5
	v_mul_f32_e32 v15, v146, v7
	v_add_f32_e32 v6, 1.0, v12
	v_rcp_f32_e32 v7, v6
	v_mul_f32_e32 v6, 0xbcb8aa3b, v155
	v_exp_f32_e32 v12, v6
	v_mul_f32_e32 v7, v7, v173
	v_mul_f32_e32 v173, v155, v5
	v_add_f32_e32 v8, 1.0, v12
	v_rcp_f32_e32 v13, v8
	v_mul_f32_e32 v8, v151, v7
	v_mul_f32_e32 v7, v13, v173
	v_mul_f32_e32 v13, 0xbcb8aa3b, v160
	v_exp_f32_e32 v13, v13
	v_mul_f32_e32 v16, v147, v7
	v_mul_f32_e32 v173, v160, v5
	v_mul_f32_e32 v12, 0xbcb8aa3b, v156
	v_add_f32_e32 v6, 1.0, v13
	v_rcp_f32_e32 v7, v6
	v_exp_f32_e32 v12, v12
	v_mul_f32_e32 v7, v7, v173
	v_mul_f32_e32 v173, v156, v5
	v_mul_f32_e32 v18, v152, v7
	v_add_f32_e32 v6, 1.0, v12
	v_rcp_f32_e32 v7, v6
	v_mul_f32_e32 v13, 0xbcb8aa3b, v161
	v_exp_f32_e32 v13, v13
	v_mul_f32_e32 v7, v7, v173
	v_mul_f32_e32 v173, v161, v5
	v_mul_f32_e32 v17, v148, v7
	v_add_f32_e32 v6, 1.0, v13
	v_rcp_f32_e32 v7, v6
	v_mul_f32_e32 v6, 0xbcb8aa3b, v157
	v_exp_f32_e32 v13, v6
	v_mul_f32_e32 v7, v7, v173
	v_mul_f32_e32 v173, v157, v5
	v_add_f32_e32 v12, 1.0, v13
	v_rcp_f32_e32 v13, v12
	v_mul_f32_e32 v20, v153, v7
	v_med3_f32 v8, v8, s60, v200
	v_mul_f32_e32 v7, v13, v173
	v_mov_b32_e32 v12, v167
	v_mul_f32_e32 v5, v149, v7
	v_med3_f32 v6, v14, s60, v200
	v_med3_f32 v7, v15, s60, v200
	v_med3_f32 v14, v16, s60, v200
	v_mov_b32_e32 v13, v167
	v_cvt_pk_fp8_f32 v12, v6, v8
	v_cvt_pk_fp8_f32 v13, v7, v14
	s_lshl_b32 s4, s36, 7
	s_or_b32 s4, s4, s54
	v_lshl_add_u32 v2, v4, 3, s4
	v_lshl_add_u32 v4, s62, 8, v11
	v_med3_f32 v15, v18, s60, v200
	v_med3_f32 v16, v17, s60, v200
	v_med3_f32 v6, v20, s60, v200
	v_med3_f32 v5, v5, s60, v200
	v_cvt_pk_fp8_f32 v12, v15, v6 op_sel:[0,0,1]
	v_cvt_pk_fp8_f32 v13, v16, v5 op_sel:[0,0,1]
	v_ashrrev_i32_e32 v5, 31, v4
	v_lshlrev_b64 v[6:7], 9, v[4:5]
	v_ashrrev_i32_e32 v3, 31, v2
	v_lshl_add_u64 v[6:7], s[18:19], 0, v[6:7]
	v_cndmask_b32_e64 v8, 0, 1, s[38:39]
	v_lshl_add_u64 v[6:7], v[6:7], 0, v[2:3]
	v_cmp_ne_u32_e64 s[4:5], 1, v8
	s_andn2_b64 vcc, exec, s[38:39]
	global_store_dwordx2 v[6:7], v[12:13], off
	s_cbranch_vccnz .LBB0_1052
	v_add3_u32 v8, s14, 16, v11
	s_waitcnt lgkmcnt(0)
	v_cmp_lt_i32_e32 vcc, v8, v10
	v_mov_b32_e32 v9, 0
	s_and_saveexec_b64 s[36:37], vcc
	s_cbranch_execz .LBB0_1051
	s_ashr_i32 s11, s10, 31
	s_lshl_b64 s[38:39], s[10:11], 15
	s_add_u32 s38, s51, s38
	s_addc_u32 s39, s52, s39
	v_ashrrev_i32_e32 v9, 31, v8
	v_lshl_add_u64 v[8:9], v[8:9], 2, s[38:39]
	global_load_dword v8, v[8:9], off
	s_waitcnt vmcnt(0)
	v_mul_f32_e32 v9, 0x3b800000, v8

.LBB0_1052:
	v_mul_f32_e32 v12, 0xbcb8aa3b, v142
	v_exp_f32_e32 v13, v12
	v_mul_f32_e32 v173, v142, v9
	v_mul_f32_e32 v8, 0xbcb8aa3b, v138
	v_add_f32_e32 v13, 1.0, v13
	v_rcp_f32_e32 v13, v13
	v_exp_f32_e32 v8, v8
	v_mul_f32_e32 v13, v13, v173
	v_add_f32_e32 v8, 1.0, v8
	v_mul_f32_e32 v16, v134, v13
	v_rcp_f32_e32 v13, v8
	v_mul_f32_e32 v173, v138, v9
	v_mul_f32_e32 v14, 0xbcb8aa3b, v143
	v_exp_f32_e32 v14, v14
	v_mul_f32_e32 v13, v13, v173
	v_mul_f32_e32 v173, v143, v9
	v_mul_f32_e32 v17, v130, v13
	v_add_f32_e32 v12, 1.0, v14
	v_rcp_f32_e32 v13, v12
	v_mul_f32_e32 v12, 0xbcb8aa3b, v139
	v_exp_f32_e32 v14, v12
	v_mul_f32_e32 v13, v13, v173
	v_mul_f32_e32 v173, v139, v9
	v_add_f32_e32 v8, 1.0, v14
	v_rcp_f32_e32 v15, v8
	v_mul_f32_e32 v19, v135, v13
	v_mul_f32_e32 v13, v15, v173
	v_mul_f32_e32 v14, 0xbcb8aa3b, v144
	v_exp_f32_e32 v14, v14
	v_mul_f32_e32 v173, v144, v9
	v_mul_f32_e32 v18, v131, v13
	v_add_f32_e32 v8, 1.0, v14
	v_rcp_f32_e32 v13, v8
	v_mul_f32_e32 v8, 0xbcb8aa3b, v140
	v_exp_f32_e32 v8, v8
	v_mul_f32_e32 v13, v13, v173
	v_mul_f32_e32 v173, v140, v9
	v_add_f32_e32 v8, 1.0, v8
	v_mul_f32_e32 v20, v136, v13
	v_rcp_f32_e32 v13, v8
	v_mul_f32_e32 v14, 0xbcb8aa3b, v145
	v_exp_f32_e32 v14, v14
	v_mul_f32_e32 v13, v13, v173
	v_mul_f32_e32 v21, v132, v13
	v_add_f32_e32 v12, 1.0, v14
	v_rcp_f32_e32 v13, v12
	v_mul_f32_e32 v12, 0xbcb8aa3b, v141
	v_exp_f32_e32 v14, v12
	v_mul_f32_e32 v173, v145, v9
	v_mul_f32_e32 v13, v13, v173
	v_add_f32_e32 v8, 1.0, v14
	v_rcp_f32_e32 v15, v8
	v_mul_f32_e32 v173, v141, v9
	v_mul_f32_e32 v12, v137, v13
	v_mul_f32_e32 v9, v15, v173
	v_med3_f32 v15, v19, s60, v200
	v_mul_f32_e32 v13, v133, v9
	v_med3_f32 v9, v16, s60, v200
	v_mov_b32_e32 v8, v167
	v_med3_f32 v14, v17, s60, v200
	v_med3_f32 v16, v18, s60, v200
	v_cvt_pk_fp8_f32 v8, v9, v15
	v_mov_b32_e32 v9, v167
	v_cvt_pk_fp8_f32 v9, v14, v16
	v_med3_f32 v17, v20, s60, v200
	v_med3_f32 v18, v21, s60, v200
	v_med3_f32 v12, v12, s60, v200
	v_med3_f32 v13, v13, s60, v200
	v_cvt_pk_fp8_f32 v8, v17, v12 op_sel:[0,0,1]
	v_cvt_pk_fp8_f32 v9, v18, v13 op_sel:[0,0,1]
	v_add_co_u32_e32 v6, vcc, 0x2000, v6
	s_nop 1
	v_addc_co_u32_e32 v7, vcc, 0, v7, vcc
	global_store_dwordx2 v[6:7], v[8:9], off
	v_mov_b32_e32 v9, 0x3b800000
	s_and_b64 vcc, exec, s[4:5]
	v_mov_b32_e32 v7, 0x3b800000
	s_cbranch_vccnz .LBB0_1056
	v_add3_u32 v6, s14, 32, v11
	s_waitcnt lgkmcnt(0)
	v_cmp_lt_i32_e32 vcc, v6, v10
	v_mov_b32_e32 v7, 0
	s_and_saveexec_b64 s[36:37], vcc
	s_cbranch_execz .LBB0_1055
	s_ashr_i32 s11, s10, 31
	s_lshl_b64 s[38:39], s[10:11], 15
	s_add_u32 s38, s51, s38
	s_addc_u32 s39, s52, s39
	v_ashrrev_i32_e32 v7, 31, v6
	v_lshl_add_u64 v[6:7], v[6:7], 2, s[38:39]
	global_load_dword v6, v[6:7], off
	s_waitcnt vmcnt(0)
	v_mul_f32_e32 v7, 0x3b800000, v6

.LBB0_1056:
	v_mul_f32_e32 v8, 0xbcb8aa3b, v126
	v_exp_f32_e32 v8, v8
	v_mul_f32_e32 v173, v126, v7
	v_mul_f32_e32 v6, 0xbcb8aa3b, v122
	v_add_f32_e32 v8, 1.0, v8
	v_rcp_f32_e32 v13, v8
	v_exp_f32_e32 v6, v6
	v_mul_f32_e32 v13, v13, v173
	v_add_f32_e32 v6, 1.0, v6
	v_mul_f32_e32 v8, v118, v13
	v_rcp_f32_e32 v13, v6
	v_mul_f32_e32 v173, v122, v7
	v_mul_f32_e32 v14, 0xbcb8aa3b, v127
	v_exp_f32_e32 v14, v14
	v_mul_f32_e32 v13, v13, v173
	v_mul_f32_e32 v173, v127, v7
	v_mul_f32_e32 v16, v114, v13
	v_add_f32_e32 v12, 1.0, v14
	v_rcp_f32_e32 v13, v12
	v_mul_f32_e32 v12, 0xbcb8aa3b, v123
	v_exp_f32_e32 v14, v12
	v_mul_f32_e32 v13, v13, v173
	v_mul_f32_e32 v173, v123, v7
	v_add_f32_e32 v6, 1.0, v14
	v_rcp_f32_e32 v15, v6
	v_mul_f32_e32 v18, v119, v13
	v_mul_f32_e32 v13, v15, v173
	v_mul_f32_e32 v14, 0xbcb8aa3b, v128
	v_exp_f32_e32 v14, v14
	v_mul_f32_e32 v173, v128, v7
	v_mul_f32_e32 v17, v115, v13
	v_add_f32_e32 v6, 1.0, v14
	v_rcp_f32_e32 v13, v6
	v_mul_f32_e32 v6, 0xbcb8aa3b, v124
	v_exp_f32_e32 v6, v6
	v_mul_f32_e32 v13, v13, v173
	v_mul_f32_e32 v173, v124, v7
	v_add_f32_e32 v6, 1.0, v6
	v_mul_f32_e32 v19, v120, v13
	v_rcp_f32_e32 v13, v6
	v_mul_f32_e32 v14, 0xbcb8aa3b, v129
	v_exp_f32_e32 v14, v14
	v_mul_f32_e32 v13, v13, v173
	v_mul_f32_e32 v20, v116, v13
	v_add_f32_e32 v12, 1.0, v14
	v_rcp_f32_e32 v13, v12
	v_mul_f32_e32 v12, 0xbcb8aa3b, v125
	v_exp_f32_e32 v14, v12
	v_mul_f32_e32 v173, v129, v7
	v_mul_f32_e32 v13, v13, v173
	v_add_f32_e32 v6, 1.0, v14
	v_rcp_f32_e32 v15, v6
	v_mul_f32_e32 v173, v125, v7
	v_mul_f32_e32 v22, v121, v13
	v_mul_f32_e32 v7, v15, v173
	v_med3_f32 v13, v18, s60, v200
	v_mul_f32_e32 v6, v117, v7
	v_med3_f32 v7, v8, s60, v200
	v_mov_b32_e32 v12, v167
	v_med3_f32 v8, v16, s60, v200
	v_med3_f32 v14, v17, s60, v200
	v_cvt_pk_fp8_f32 v12, v7, v13
	v_mov_b32_e32 v13, v167
	v_cvt_pk_fp8_f32 v13, v8, v14
	v_med3_f32 v15, v19, s60, v200
	v_med3_f32 v16, v20, s60, v200
	v_med3_f32 v7, v22, s60, v200
	v_med3_f32 v6, v6, s60, v200
	v_cvt_pk_fp8_f32 v12, v15, v7 op_sel:[0,0,1]
	v_cvt_pk_fp8_f32 v13, v16, v6 op_sel:[0,0,1]
	v_lshlrev_b64 v[6:7], 9, v[4:5]
	v_lshl_add_u64 v[6:7], s[18:19], 0, v[6:7]
	v_lshl_add_u64 v[6:7], v[6:7], 0, v[2:3]
	v_add_co_u32_e32 v14, vcc, 0x4000, v6
	s_nop 1
	v_addc_co_u32_e32 v15, vcc, 0, v7, vcc
	s_and_b64 vcc, exec, s[4:5]
	global_store_dwordx2 v[14:15], v[12:13], off
	s_cbranch_vccnz .LBB0_1060
	v_add3_u32 v8, s14, 48, v11
	s_waitcnt lgkmcnt(0)
	v_cmp_lt_i32_e32 vcc, v8, v10
	v_mov_b32_e32 v9, 0
	s_and_saveexec_b64 s[36:37], vcc
	s_cbranch_execz .LBB0_1059
	s_ashr_i32 s11, s10, 31
	s_lshl_b64 s[38:39], s[10:11], 15
	s_add_u32 s38, s51, s38
	s_addc_u32 s39, s52, s39
	v_ashrrev_i32_e32 v9, 31, v8
	v_lshl_add_u64 v[8:9], v[8:9], 2, s[38:39]
	global_load_dword v8, v[8:9], off
	s_waitcnt vmcnt(0)
	v_mul_f32_e32 v9, 0x3b800000, v8

.LBB0_1060:
	v_mul_f32_e32 v12, 0xbcb8aa3b, v110
	v_exp_f32_e32 v13, v12
	v_mul_f32_e32 v173, v110, v9
	v_mul_f32_e32 v8, 0xbcb8aa3b, v106
	v_add_f32_e32 v13, 1.0, v13
	v_rcp_f32_e32 v13, v13
	v_exp_f32_e32 v8, v8
	v_mul_f32_e32 v13, v13, v173
	v_add_f32_e32 v8, 1.0, v8
	v_mul_f32_e32 v16, v102, v13
	v_rcp_f32_e32 v13, v8
	v_mul_f32_e32 v173, v106, v9
	v_mul_f32_e32 v14, 0xbcb8aa3b, v111
	v_exp_f32_e32 v14, v14
	v_mul_f32_e32 v13, v13, v173
	v_mul_f32_e32 v173, v111, v9
	v_mul_f32_e32 v17, v98, v13
	v_add_f32_e32 v12, 1.0, v14
	v_rcp_f32_e32 v13, v12
	v_mul_f32_e32 v12, 0xbcb8aa3b, v107
	v_exp_f32_e32 v14, v12
	v_mul_f32_e32 v13, v13, v173
	v_mul_f32_e32 v173, v107, v9
	v_add_f32_e32 v8, 1.0, v14
	v_rcp_f32_e32 v15, v8
	v_mul_f32_e32 v19, v103, v13
	v_mul_f32_e32 v13, v15, v173
	v_mul_f32_e32 v14, 0xbcb8aa3b, v112
	v_exp_f32_e32 v14, v14
	v_mul_f32_e32 v173, v112, v9
	v_mul_f32_e32 v18, v99, v13
	v_add_f32_e32 v8, 1.0, v14
	v_rcp_f32_e32 v13, v8
	v_mul_f32_e32 v8, 0xbcb8aa3b, v108
	v_exp_f32_e32 v8, v8
	v_mul_f32_e32 v13, v13, v173
	v_mul_f32_e32 v173, v108, v9
	v_add_f32_e32 v8, 1.0, v8
	v_mul_f32_e32 v20, v104, v13
	v_rcp_f32_e32 v13, v8
	v_mul_f32_e32 v14, 0xbcb8aa3b, v113
	v_exp_f32_e32 v14, v14
	v_mul_f32_e32 v13, v13, v173
	v_mul_f32_e32 v21, v100, v13
	v_add_f32_e32 v12, 1.0, v14
	v_rcp_f32_e32 v13, v12
	v_mul_f32_e32 v12, 0xbcb8aa3b, v109
	v_exp_f32_e32 v14, v12
	v_mul_f32_e32 v173, v113, v9
	v_mul_f32_e32 v13, v13, v173
	v_add_f32_e32 v8, 1.0, v14
	v_rcp_f32_e32 v15, v8
	v_mul_f32_e32 v173, v109, v9
	v_mul_f32_e32 v12, v105, v13
	v_mul_f32_e32 v9, v15, v173
	v_med3_f32 v15, v19, s60, v200
	v_mul_f32_e32 v13, v101, v9
	v_med3_f32 v9, v16, s60, v200
	v_mov_b32_e32 v8, v167
	v_med3_f32 v14, v17, s60, v200
	v_med3_f32 v16, v18, s60, v200
	v_cvt_pk_fp8_f32 v8, v9, v15
	v_mov_b32_e32 v9, v167
	v_cvt_pk_fp8_f32 v9, v14, v16
	v_med3_f32 v17, v20, s60, v200
	v_med3_f32 v18, v21, s60, v200
	v_med3_f32 v12, v12, s60, v200
	v_med3_f32 v13, v13, s60, v200
	v_cvt_pk_fp8_f32 v8, v17, v12 op_sel:[0,0,1]
	v_cvt_pk_fp8_f32 v9, v18, v13 op_sel:[0,0,1]
	v_add_co_u32_e32 v6, vcc, 0x6000, v6
	s_nop 1
	v_addc_co_u32_e32 v7, vcc, 0, v7, vcc
	global_store_dwordx2 v[6:7], v[8:9], off
	v_mov_b32_e32 v9, 0x3b800000
	s_and_b64 vcc, exec, s[4:5]
	v_mov_b32_e32 v7, 0x3b800000
	s_cbranch_vccnz .LBB0_1064
	s_add_i32 s11, s14, 0x80
	v_add_u32_e32 v6, s11, v11
	s_waitcnt lgkmcnt(0)
	v_cmp_lt_i32_e32 vcc, v6, v10
	v_mov_b32_e32 v7, 0
	s_and_saveexec_b64 s[36:37], vcc
	s_cbranch_execz .LBB0_1063
	s_ashr_i32 s11, s10, 31
	s_lshl_b64 s[38:39], s[10:11], 15
	s_add_u32 s38, s51, s38
	s_addc_u32 s39, s52, s39
	v_ashrrev_i32_e32 v7, 31, v6
	v_lshl_add_u64 v[6:7], v[6:7], 2, s[38:39]
	global_load_dword v6, v[6:7], off
	s_waitcnt vmcnt(0)
	v_mul_f32_e32 v7, 0x3b800000, v6

.LBB0_1064:
	v_mul_f32_e32 v8, 0xbcb8aa3b, v94
	v_exp_f32_e32 v8, v8
	v_mul_f32_e32 v173, v94, v7
	v_mul_f32_e32 v6, 0xbcb8aa3b, v90
	v_add_f32_e32 v8, 1.0, v8
	v_rcp_f32_e32 v13, v8
	v_exp_f32_e32 v6, v6
	v_mul_f32_e32 v13, v13, v173
	v_add_f32_e32 v6, 1.0, v6
	v_mul_f32_e32 v8, v86, v13
	v_rcp_f32_e32 v13, v6
	v_mul_f32_e32 v173, v90, v7
	v_mul_f32_e32 v14, 0xbcb8aa3b, v95
	v_exp_f32_e32 v14, v14
	v_mul_f32_e32 v13, v13, v173
	v_mul_f32_e32 v173, v95, v7
	v_mul_f32_e32 v16, v82, v13
	v_add_f32_e32 v12, 1.0, v14
	v_rcp_f32_e32 v13, v12
	v_mul_f32_e32 v12, 0xbcb8aa3b, v91
	v_exp_f32_e32 v14, v12
	v_mul_f32_e32 v13, v13, v173
	v_mul_f32_e32 v173, v91, v7
	v_add_f32_e32 v6, 1.0, v14
	v_rcp_f32_e32 v15, v6
	v_mul_f32_e32 v18, v87, v13
	v_mul_f32_e32 v13, v15, v173
	v_mul_f32_e32 v14, 0xbcb8aa3b, v96
	v_exp_f32_e32 v14, v14
	v_mul_f32_e32 v173, v96, v7
	v_mul_f32_e32 v17, v83, v13
	v_add_f32_e32 v6, 1.0, v14
	v_rcp_f32_e32 v13, v6
	v_mul_f32_e32 v6, 0xbcb8aa3b, v92
	v_exp_f32_e32 v6, v6
	v_mul_f32_e32 v13, v13, v173
	v_mul_f32_e32 v173, v92, v7
	v_add_f32_e32 v6, 1.0, v6
	v_mul_f32_e32 v19, v88, v13
	v_rcp_f32_e32 v13, v6
	v_mul_f32_e32 v14, 0xbcb8aa3b, v97
	v_exp_f32_e32 v14, v14
	v_mul_f32_e32 v13, v13, v173
	v_mul_f32_e32 v20, v84, v13
	v_add_f32_e32 v12, 1.0, v14
	v_rcp_f32_e32 v13, v12
	v_mul_f32_e32 v12, 0xbcb8aa3b, v93
	v_exp_f32_e32 v14, v12
	v_mul_f32_e32 v173, v97, v7
	v_mul_f32_e32 v13, v13, v173
	v_add_f32_e32 v6, 1.0, v14
	v_rcp_f32_e32 v15, v6
	v_mul_f32_e32 v173, v93, v7
	v_mul_f32_e32 v22, v89, v13
	v_mul_f32_e32 v7, v15, v173
	v_med3_f32 v13, v18, s60, v200
	v_mul_f32_e32 v6, v85, v7
	v_med3_f32 v7, v8, s60, v200
	v_mov_b32_e32 v12, v167
	v_med3_f32 v8, v16, s60, v200
	v_med3_f32 v14, v17, s60, v200
	v_cvt_pk_fp8_f32 v12, v7, v13
	v_mov_b32_e32 v13, v167
	v_cvt_pk_fp8_f32 v13, v8, v14
	v_med3_f32 v15, v19, s60, v200
	v_med3_f32 v16, v20, s60, v200
	v_med3_f32 v7, v22, s60, v200
	v_med3_f32 v6, v6, s60, v200
	v_cvt_pk_fp8_f32 v12, v15, v7 op_sel:[0,0,1]
	v_cvt_pk_fp8_f32 v13, v16, v6 op_sel:[0,0,1]
	v_lshlrev_b64 v[6:7], 9, v[4:5]
	v_lshl_add_u64 v[6:7], s[18:19], 0, v[6:7]
	v_lshl_add_u64 v[6:7], v[6:7], 0, v[2:3]
	v_add_co_u32_e32 v14, vcc, 0x10000, v6
	s_nop 1
	v_addc_co_u32_e32 v15, vcc, 0, v7, vcc
	s_and_b64 vcc, exec, s[4:5]
	global_store_dwordx2 v[14:15], v[12:13], off
	s_cbranch_vccnz .LBB0_1068
	s_add_i32 s11, s14, 0x90
	v_add_u32_e32 v8, s11, v11
	s_waitcnt lgkmcnt(0)
	v_cmp_lt_i32_e32 vcc, v8, v10
	v_mov_b32_e32 v9, 0
	s_and_saveexec_b64 s[36:37], vcc
	s_cbranch_execz .LBB0_1067
	s_ashr_i32 s11, s10, 31
	s_lshl_b64 s[38:39], s[10:11], 15
	s_add_u32 s38, s51, s38
	s_addc_u32 s39, s52, s39
	v_ashrrev_i32_e32 v9, 31, v8
	v_lshl_add_u64 v[8:9], v[8:9], 2, s[38:39]
	global_load_dword v8, v[8:9], off
	s_waitcnt vmcnt(0)
	v_mul_f32_e32 v9, 0x3b800000, v8

.LBB0_1068:
	v_mul_f32_e32 v12, 0xbcb8aa3b, v78
	v_exp_f32_e32 v13, v12
	v_mul_f32_e32 v173, v78, v9
	v_mul_f32_e32 v8, 0xbcb8aa3b, v74
	v_add_f32_e32 v13, 1.0, v13
	v_rcp_f32_e32 v13, v13
	v_exp_f32_e32 v8, v8
	v_mul_f32_e32 v13, v13, v173
	v_add_f32_e32 v8, 1.0, v8
	v_mul_f32_e32 v16, v70, v13
	v_rcp_f32_e32 v13, v8
	v_mul_f32_e32 v173, v74, v9
	v_mul_f32_e32 v14, 0xbcb8aa3b, v79
	v_exp_f32_e32 v14, v14
	v_mul_f32_e32 v13, v13, v173
	v_mul_f32_e32 v173, v79, v9
	v_mul_f32_e32 v17, v66, v13
	v_add_f32_e32 v12, 1.0, v14
	v_rcp_f32_e32 v13, v12
	v_mul_f32_e32 v12, 0xbcb8aa3b, v75
	v_exp_f32_e32 v14, v12
	v_mul_f32_e32 v13, v13, v173
	v_mul_f32_e32 v173, v75, v9
	v_add_f32_e32 v8, 1.0, v14
	v_rcp_f32_e32 v15, v8
	v_mul_f32_e32 v19, v71, v13
	v_mul_f32_e32 v13, v15, v173
	v_mul_f32_e32 v14, 0xbcb8aa3b, v80
	v_exp_f32_e32 v14, v14
	v_mul_f32_e32 v173, v80, v9
	v_mul_f32_e32 v18, v67, v13
	v_add_f32_e32 v8, 1.0, v14
	v_rcp_f32_e32 v13, v8
	v_mul_f32_e32 v8, 0xbcb8aa3b, v76
	v_exp_f32_e32 v8, v8
	v_mul_f32_e32 v13, v13, v173
	v_mul_f32_e32 v173, v76, v9
	v_add_f32_e32 v8, 1.0, v8
	v_mul_f32_e32 v20, v72, v13
	v_rcp_f32_e32 v13, v8
	v_mul_f32_e32 v14, 0xbcb8aa3b, v81
	v_exp_f32_e32 v14, v14
	v_mul_f32_e32 v13, v13, v173
	v_mul_f32_e32 v21, v68, v13
	v_add_f32_e32 v12, 1.0, v14
	v_rcp_f32_e32 v13, v12
	v_mul_f32_e32 v12, 0xbcb8aa3b, v77
	v_exp_f32_e32 v14, v12
	v_mul_f32_e32 v173, v81, v9
	v_mul_f32_e32 v13, v13, v173
	v_add_f32_e32 v8, 1.0, v14
	v_rcp_f32_e32 v15, v8
	v_mul_f32_e32 v173, v77, v9
	v_mul_f32_e32 v12, v73, v13
	v_mul_f32_e32 v9, v15, v173
	v_med3_f32 v15, v19, s60, v200
	v_mul_f32_e32 v13, v69, v9
	v_med3_f32 v9, v16, s60, v200
	v_mov_b32_e32 v8, v167
	v_med3_f32 v14, v17, s60, v200
	v_med3_f32 v16, v18, s60, v200
	v_cvt_pk_fp8_f32 v8, v9, v15
	v_mov_b32_e32 v9, v167
	v_cvt_pk_fp8_f32 v9, v14, v16
	v_med3_f32 v17, v20, s60, v200
	v_med3_f32 v18, v21, s60, v200
	v_med3_f32 v12, v12, s60, v200
	v_med3_f32 v13, v13, s60, v200
	v_cvt_pk_fp8_f32 v8, v17, v12 op_sel:[0,0,1]
	v_cvt_pk_fp8_f32 v9, v18, v13 op_sel:[0,0,1]
	v_add_co_u32_e32 v6, vcc, 0x12000, v6
	s_nop 1
	v_addc_co_u32_e32 v7, vcc, 0, v7, vcc
	global_store_dwordx2 v[6:7], v[8:9], off
	v_mov_b32_e32 v8, 0x3b800000
	s_and_b64 vcc, exec, s[4:5]
	v_mov_b32_e32 v7, 0x3b800000
	s_cbranch_vccnz .LBB0_1072
	s_add_i32 s11, s14, 0xa0
	v_add_u32_e32 v6, s11, v11
	s_waitcnt lgkmcnt(0)
	v_cmp_lt_i32_e32 vcc, v6, v10
	v_mov_b32_e32 v7, 0
	s_and_saveexec_b64 s[36:37], vcc
	s_cbranch_execz .LBB0_1071
	s_ashr_i32 s11, s10, 31
	s_lshl_b64 s[38:39], s[10:11], 15
	s_add_u32 s38, s51, s38
	s_addc_u32 s39, s52, s39
	v_ashrrev_i32_e32 v7, 31, v6
	v_lshl_add_u64 v[6:7], v[6:7], 2, s[38:39]
	global_load_dword v6, v[6:7], off
	s_waitcnt vmcnt(0)
	v_mul_f32_e32 v7, 0x3b800000, v6

.LBB0_1072:
	v_mul_f32_e32 v9, 0xbcb8aa3b, v54
	v_exp_f32_e32 v9, v9
	v_mul_f32_e32 v173, v54, v7
	v_mul_f32_e32 v6, 0xbcb8aa3b, v50
	v_add_f32_e32 v9, 1.0, v9
	v_rcp_f32_e32 v13, v9
	v_exp_f32_e32 v6, v6
	v_mul_f32_e32 v13, v13, v173
	v_add_f32_e32 v6, 1.0, v6
	v_mul_f32_e32 v9, v62, v13
	v_rcp_f32_e32 v13, v6
	v_mul_f32_e32 v173, v50, v7
	v_mul_f32_e32 v14, 0xbcb8aa3b, v55
	v_exp_f32_e32 v14, v14
	v_mul_f32_e32 v13, v13, v173
	v_mul_f32_e32 v173, v55, v7
	v_mul_f32_e32 v16, v58, v13
	v_add_f32_e32 v12, 1.0, v14
	v_rcp_f32_e32 v13, v12
	v_mul_f32_e32 v12, 0xbcb8aa3b, v51
	v_exp_f32_e32 v14, v12
	v_mul_f32_e32 v13, v13, v173
	v_mul_f32_e32 v173, v51, v7
	v_add_f32_e32 v6, 1.0, v14
	v_rcp_f32_e32 v15, v6
	v_mul_f32_e32 v18, v63, v13
	v_mul_f32_e32 v13, v15, v173
	v_mul_f32_e32 v14, 0xbcb8aa3b, v56
	v_exp_f32_e32 v14, v14
	v_mul_f32_e32 v173, v56, v7
	v_mul_f32_e32 v17, v59, v13
	v_add_f32_e32 v6, 1.0, v14
	v_rcp_f32_e32 v13, v6
	v_mul_f32_e32 v6, 0xbcb8aa3b, v52
	v_exp_f32_e32 v6, v6
	v_mul_f32_e32 v13, v13, v173
	v_mul_f32_e32 v173, v52, v7
	v_add_f32_e32 v6, 1.0, v6
	v_mul_f32_e32 v19, v64, v13
	v_rcp_f32_e32 v13, v6
	v_mul_f32_e32 v14, 0xbcb8aa3b, v57
	v_exp_f32_e32 v14, v14
	v_mul_f32_e32 v13, v13, v173
	v_mul_f32_e32 v20, v60, v13
	v_add_f32_e32 v12, 1.0, v14
	v_rcp_f32_e32 v13, v12
	v_mul_f32_e32 v12, 0xbcb8aa3b, v53
	v_exp_f32_e32 v14, v12
	v_mul_f32_e32 v173, v57, v7
	v_mul_f32_e32 v13, v13, v173
	v_add_f32_e32 v6, 1.0, v14
	v_rcp_f32_e32 v15, v6
	v_mul_f32_e32 v173, v53, v7
	v_mul_f32_e32 v12, v65, v13
	v_mul_f32_e32 v7, v15, v173
	v_med3_f32 v14, v18, s60, v200
	v_mul_f32_e32 v13, v61, v7
	v_med3_f32 v7, v9, s60, v200
	v_mov_b32_e32 v6, v167
	v_med3_f32 v9, v16, s60, v200
	v_med3_f32 v15, v17, s60, v200
	v_cvt_pk_fp8_f32 v6, v7, v14
	v_mov_b32_e32 v7, v167
	v_cvt_pk_fp8_f32 v7, v9, v15
	v_lshlrev_b64 v[4:5], 9, v[4:5]
	v_med3_f32 v16, v19, s60, v200
	v_med3_f32 v17, v20, s60, v200
	v_med3_f32 v9, v12, s60, v200
	v_med3_f32 v12, v13, s60, v200
	v_lshl_add_u64 v[4:5], s[18:19], 0, v[4:5]
	v_cvt_pk_fp8_f32 v6, v16, v9 op_sel:[0,0,1]
	v_cvt_pk_fp8_f32 v7, v17, v12 op_sel:[0,0,1]
	v_lshl_add_u64 v[2:3], v[4:5], 0, v[2:3]
	v_add_co_u32_e32 v4, vcc, 0x14000, v2
	s_nop 1
	v_addc_co_u32_e32 v5, vcc, 0, v3, vcc
	s_and_b64 vcc, exec, s[4:5]
	global_store_dwordx2 v[4:5], v[6:7], off
	s_cbranch_vccnz .LBB0_1076
	s_add_i32 s4, s14, 0xb0
	v_add_u32_e32 v4, s4, v11
	s_waitcnt lgkmcnt(0)
	v_cmp_lt_i32_e32 vcc, v4, v10
	v_mov_b32_e32 v8, 0
	s_and_saveexec_b64 s[4:5], vcc
	s_cbranch_execz .LBB0_1075
	s_ashr_i32 s11, s10, 31
	s_lshl_b64 s[10:11], s[10:11], 15
	s_add_u32 s10, s51, s10
	s_addc_u32 s11, s52, s11
	v_ashrrev_i32_e32 v5, 31, v4
	v_lshl_add_u64 v[4:5], v[4:5], 2, s[10:11]
	global_load_dword v4, v[4:5], off
	s_waitcnt vmcnt(0)
	v_mul_f32_e32 v8, 0x3b800000, v4

.LBB0_1076:
	v_mul_f32_e32 v4, 0xbcb8aa3b, v38
	v_exp_f32_e32 v5, v4
	v_mul_f32_e32 v173, v38, v8
	v_mul_f32_e32 v6, 0xbcb8aa3b, v34
	v_add_f32_e32 v5, 1.0, v5
	v_rcp_f32_e32 v5, v5
	v_exp_f32_e32 v6, v6
	v_mul_f32_e32 v5, v5, v173
	v_mul_f32_e32 v173, v34, v8
	v_mul_f32_e32 v9, v46, v5
	v_add_f32_e32 v4, 1.0, v6
	v_rcp_f32_e32 v5, v4
	v_mul_f32_e32 v7, 0xbcb8aa3b, v39
	v_exp_f32_e32 v7, v7
	v_mul_f32_e32 v5, v5, v173
	v_mul_f32_e32 v173, v39, v8
	s_waitcnt lgkmcnt(0)
	v_mul_f32_e32 v10, v42, v5
	v_add_f32_e32 v4, 1.0, v7
	v_rcp_f32_e32 v5, v4
	v_mul_f32_e32 v4, 0xbcb8aa3b, v35
	v_exp_f32_e32 v7, v4
	v_mul_f32_e32 v5, v5, v173
	v_mul_f32_e32 v173, v35, v8
	v_add_f32_e32 v6, 1.0, v7
	v_rcp_f32_e32 v7, v6
	v_mul_f32_e32 v12, v47, v5
	v_mul_f32_e32 v5, v7, v173
	v_mul_f32_e32 v7, 0xbcb8aa3b, v40
	v_exp_f32_e32 v7, v7
	v_mul_f32_e32 v11, v43, v5
	v_mul_f32_e32 v173, v40, v8
	v_mul_f32_e32 v6, 0xbcb8aa3b, v36
	v_add_f32_e32 v4, 1.0, v7
	v_rcp_f32_e32 v5, v4
	v_exp_f32_e32 v6, v6
	v_mul_f32_e32 v5, v5, v173
	v_mul_f32_e32 v173, v36, v8
	v_mul_f32_e32 v14, v48, v5
	v_add_f32_e32 v4, 1.0, v6
	v_rcp_f32_e32 v5, v4
	v_mul_f32_e32 v7, 0xbcb8aa3b, v41
	v_exp_f32_e32 v7, v7
	v_mul_f32_e32 v5, v5, v173
	v_mul_f32_e32 v173, v41, v8
	v_mul_f32_e32 v13, v44, v5
	v_add_f32_e32 v4, 1.0, v7
	v_rcp_f32_e32 v5, v4
	v_mul_f32_e32 v4, 0xbcb8aa3b, v37
	v_exp_f32_e32 v7, v4
	v_mul_f32_e32 v5, v5, v173
	v_mul_f32_e32 v173, v37, v8
	v_add_f32_e32 v6, 1.0, v7
	v_rcp_f32_e32 v7, v6
	v_mul_f32_e32 v16, v49, v5
	v_med3_f32 v8, v12, s60, v200
	v_mul_f32_e32 v5, v7, v173
	v_med3_f32 v7, v10, s60, v200
	v_mul_f32_e32 v6, v45, v5
	v_med3_f32 v5, v9, s60, v200
	v_mov_b32_e32 v4, v167
	v_med3_f32 v9, v11, s60, v200
	v_cvt_pk_fp8_f32 v4, v5, v8
	v_mov_b32_e32 v5, v167
	v_cvt_pk_fp8_f32 v5, v7, v9
	v_med3_f32 v10, v14, s60, v200
	v_med3_f32 v11, v13, s60, v200
	v_med3_f32 v7, v16, s60, v200
	v_med3_f32 v6, v6, s60, v200
	v_cvt_pk_fp8_f32 v4, v10, v7 op_sel:[0,0,1]
	v_cvt_pk_fp8_f32 v5, v11, v6 op_sel:[0,0,1]
	v_add_co_u32_e32 v2, vcc, 0x16000, v2
	s_nop 1
	v_addc_co_u32_e32 v3, vcc, 0, v3, vcc
	s_and_b64 vcc, exec, s[0:1]
	s_mov_b64 s[0:1], -1
	global_store_dwordx2 v[2:3], v[4:5], off
	s_cbranch_vccnz .LBB0_1019
	s_andn2_b64 vcc, exec, s[16:17]
	s_cbranch_vccnz .LBB0_1018
	s_barrier
	s_branch .LBB0_1018
